# workgroups without a fifth in-projection tile convert one weight item per wave of the next layer before the A to B grid barrier (B's conversion loop then skips it)
# baseline (speedup 1.0000x reference)
; #define PH_IDS() int lane_ = lane_id(); asm volatile("" : "+v"(lane_)); const int lane = lane_; const int wave = wave_s; const int tid = wave * 64 + lane; const int gw = vcu * 8 + wave; (void)lane; (void)gw; (void)tid
; __global__ void __launch_bounds__(512, 2) mega(Args a) {
;     ...
; #pragma unroll 1
;     for (int l = 0; l < NLAYER; ++l) {
;         const int pb = 2 + 10 * l;
;         const float* MODL = MOD + (size_t)l * 5 * 6144;
;         for (int rep_ = 0; rep_ < REPS(0); ++rep_) if (EN(0) && IN(pb + 0)) { PH_IDS();
.LBB0_127:
	s_waitcnt lgkmcnt(0)
	s_barrier
	s_mov_b32 s0, 0
	v_writelane_b32 v255, s0, 44
	v_writelane_b32 v255, s0, 45
	v_writelane_b32 v255, s0, 47
	s_nop 1

; #define LAS __attribute__((address_space(3)))
; #define SEAM(k) do { if (IN(k) && IN((k) + 1)) xcd_barrier(bar); } while (0)
; __global__ void __launch_bounds__(512, 2) mega(Args a) {
;     ...
;         SEAM(pb + 0);
;     ...
;             if (l + 1 < NLAYER && vcu >= 8) {
;                 LAS float* scr = (LAS float*)(lds + wave * 16384);
;                 for (int it = (vcu - 8) * 8 + wave; it < IT_LAYER / 2; it += (G - 8) * 8) CONVERT_ITEM(l + 1, it);
;             }
.LBB0_210:
	s_waitcnt vmcnt(0)
	s_barrier
	v_readlane_b32 s0, v254, 52
	s_nop 3
	s_cmp_eq_u32 s0, 3
	s_cbranch_scc1 .LBB0_211
	v_readlane_b32 s0, v246, 4
	s_nop 3
	s_cmp_lt_u32 s0, 8
	s_cbranch_scc1 .LBB0_211
	s_and_b32 s0, s0, 31
	s_cmp_lt_u32 s0, 4
	s_cbranch_scc1 .LBB0_211
	s_mov_b32 s0, 5
	v_writelane_b32 v255, s0, 44
	s_mov_b64 s[6:7], exec
	s_nop 1
	s_branch .Lb_reenter

; #define LAS __attribute__((address_space(3)))
; __global__ void __launch_bounds__(512, 2) mega(Args a) {
;     ...
;             if (l + 1 < NLAYER && vcu >= 8) {
;                 LAS float* scr = (LAS float*)(lds + wave * 16384);
;                 for (int it = (vcu - 8) * 8 + wave; it < IT_LAYER / 2; it += (G - 8) * 8) CONVERT_ITEM(l + 1, it);
;             }
.Lb_reenter:
	v_readlane_b32 s0, v254, 52
	s_lshl_b32 s62, s0, 8
	s_lshl_b32 s23, s0, 2
	s_cmp_eq_u32 s0, 3
	s_cselect_b64 s[2:3], -1, 0
	v_readlane_b32 s1, v254, 53
	v_writelane_b32 v254, s2, 56
	s_cmp_lg_u32 s0, 3
	v_readlane_b32 s40, v253, 58
	v_writelane_b32 v254, s3, 57
	s_cselect_b64 s[2:3], -1, 0
	s_add_i32 s16, s0, 1
	v_readlane_b32 s0, v253, 32
	v_readlane_b32 s1, v253, 33
	s_mov_b32 s5, s1
	s_lshl_b32 s4, s16, 20
	s_lshl_b32 s21, s16, 5
	s_lshl_b64 s[0:1], s[4:5], 2
	v_writelane_b32 v254, s2, 58
	v_readlane_b32 s41, v253, 59
	s_add_u32 s0, s40, s0
	v_writelane_b32 v254, s3, 59
	s_addc_u32 s1, s41, s1
	v_readlane_b32 s46, v254, 0
	v_readlane_b32 s47, v254, 1
	v_readlane_b32 s48, v254, 2
	v_readlane_b32 s49, v254, 3
	v_readlane_b32 s50, v254, 4
	v_readlane_b32 s51, v254, 5
	v_readlane_b32 s52, v254, 6
	v_readlane_b32 s53, v254, 7
	v_readlane_b32 s54, v254, 8
	v_readlane_b32 s55, v254, 9
	v_writelane_b32 v254, s0, 60
	v_readlane_b32 s2, v246, 13
	v_readlane_b32 s3, v246, 14
	v_writelane_b32 v254, s1, 61
	s_lshl_b32 s0, s16, 21
	s_add_u32 s0, s2, s0
	s_addc_u32 s1, s3, 0
	v_writelane_b32 v254, s0, 62
	v_readlane_b32 s42, v253, 60
	v_readlane_b32 s43, v253, 61
	v_writelane_b32 v254, s1, 63
	s_mov_b32 s1, s5
	v_readlane_b32 s44, v253, 62
	v_readlane_b32 s45, v253, 63
	v_writelane_b32 v253, s0, 32
	s_mov_b32 s17, s5
	v_readlane_b32 s2, v246, 11
	v_writelane_b32 v253, s1, 33
	s_lshl_b64 s[0:1], s[16:17], 20
	v_readlane_b32 s8, v253, 38
	v_readlane_b32 s9, v253, 39
	s_add_u32 s0, s8, s0
	s_addc_u32 s1, s9, s1
	v_writelane_b32 v255, s0, 0
	v_readlane_b32 s3, v246, 12
	v_readlane_b32 s10, v253, 40
	v_writelane_b32 v255, s1, 1
	s_lshl_b64 s[0:1], s[16:17], 19
	s_add_u32 s0, s2, s0
	v_readlane_b32 s11, v253, 41
	s_addc_u32 s1, s3, s1
	v_writelane_b32 v255, s0, 2
	v_readlane_b32 s8, v253, 42
	v_readlane_b32 s14, v253, 48
	v_writelane_b32 v255, s1, 3
	s_mul_i32 s1, s16, 0x120000
	s_mul_hi_u32 s0, s16, 0x120000
	v_readlane_b32 s15, v253, 49
	s_add_u32 s2, s14, s1
	s_addc_u32 s3, s15, s0
	v_writelane_b32 v255, s2, 4
	s_mul_i32 s1, s16, 0x90000
	s_mul_hi_u32 s0, s16, 0x90000
	v_writelane_b32 v255, s3, 5
	v_readlane_b32 s2, v246, 9
	v_readlane_b32 s3, v246, 10
	s_add_u32 s2, s2, s1
	s_addc_u32 s3, s3, s0
	v_writelane_b32 v255, s2, 6
	s_mul_i32 s1, s16, 0x7c0000
	v_readlane_b32 s9, v253, 43
	v_writelane_b32 v255, s3, 7
	s_mul_hi_u32 s0, s16, 0x7c0000
	s_add_u32 s2, s8, s1
	s_addc_u32 s3, s9, s0
	v_writelane_b32 v255, s2, 8
	s_mov_b32 s0, s16
	v_readlane_b32 s10, v253, 44
	v_writelane_b32 v255, s3, 9
	v_writelane_b32 v255, s0, 10
	v_readlane_b32 s2, v246, 7
	v_readlane_b32 s3, v246, 8
	v_writelane_b32 v255, s1, 11
	s_lshl_b64 s[0:1], s[16:17], 21
	s_add_u32 s0, s2, s0
	s_addc_u32 s1, s3, s1
	v_writelane_b32 v255, s0, 12
	s_andn2_b64 vcc, exec, s[6:7]
	v_readlane_b32 s11, v253, 45
	v_writelane_b32 v255, s1, 13
	v_readlane_b32 s0, v247, 63
	v_readlane_b32 s1, v248, 0
	v_readlane_b32 s12, v253, 46
	v_readlane_b32 s13, v253, 47
	s_waitcnt vmcnt(0)
	v_cndmask_b32_e64 v0, 0, 1, s[0:1]
	v_cmp_ne_u32_e64 s[84:85], 1, v0
	s_cbranch_vccnz .LBB0_364
	v_mbcnt_lo_u32_b32 v100, -1, 0
	v_mbcnt_hi_u32_b32 v100, -1, v100
	s_and_b64 vcc, exec, s[84:85]
	s_nop 0
	v_and_b32_e32 v97, 31, v100
	v_ashrrev_i32_e32 v96, 5, v100
	v_lshlrev_b32_e32 v98, 2, v97
	s_cbranch_vccnz .LBB0_328
	v_readlane_b32 s0, v255, 44
	s_nop 3
	s_cmp_eq_u32 s0, 5
	s_cbranch_scc1 .LBB0_328
	s_cmp_lg_u32 s0, 0
	s_cbranch_scc1 .Lb_chunk
	v_readlane_b32 s0, v246, 4
	s_nop 3
	s_bitcmp1_b32 s0, 0
	s_cbranch_scc0 .Lb_chunk
	v_readlane_b32 s0, v248, 13
	s_nop 3
	s_cmp_lg_u32 s0, 0
	s_cbranch_scc1 .Lb_chunk
	v_readlane_b32 s0, v254, 56
	s_nop 3
	s_cmp_lg_u32 s0, 0
	s_cbranch_scc1 .Lb_chunk
	v_readlane_b32 s0, v248, 16
	s_nop 3
	s_cmp_lg_u32 s0, 0
	s_cbranch_scc1 .Lb_chunk
	s_mov_b32 s0, 2
	v_writelane_b32 v255, s0, 44
	s_nop 1
	s_branch .LBB0_328

; #define LAS __attribute__((address_space(3)))
; __device__ __forceinline__ unsigned pk4_fp8(float x0, float x1, float x2, float x3) { int w = 0; w = __builtin_amdgcn_cvt_pk_fp8_f32(x0, x1, w, false); w = __builtin_amdgcn_cvt_pk_fp8_f32(x2, x3, w, true); return (unsigned)w; }
; __device__ __forceinline__ void transpose_item_fp8w(const float* W, int K, int N, unsigned char* WT, float q, LAS unsigned char* scr, int item, int lane) {
;     const int nblk = N / 128, kb = item / nblk, nb = item % nblk, k0 = 64 * kb, n0 = 128 * nb;
;     const int l5 = lane & 31, h = lane >> 5;
;     const float* src = W + (size_t)(k0 + 16 * h) * N + n0 + 4 * l5;
; #pragma unroll
;     for (int b = 0; b < 2; ++b) {
;         f32x4 x[16];
; #pragma unroll
;         for (int s_ = 0; s_ < 16; ++s_) x[s_] = *(const f32x4*)(src + (size_t)(32 * b + s_) * N);
; #pragma unroll
;         for (int i = 0; i < 4; ++i) {
;             u32x4 o;
;             o.x = pk4_fp8(x[0][i] * q, x[1][i] * q, x[2][i] * q, x[3][i] * q); o.y = pk4_fp8(x[4][i] * q, x[5][i] * q, x[6][i] * q, x[7][i] * q);
;             o.z = pk4_fp8(x[8][i] * q, x[9][i] * q, x[10][i] * q, x[11][i] * q); o.w = pk4_fp8(x[12][i] * q, x[13][i] * q, x[14][i] * q, x[15][i] * q);
;             *(LAS u32x4*)(scr + (l5 + 32 * i) * 80 + (2 * b + h) * 16) = o; }
;     }
;     asm volatile("s_waitcnt lgkmcnt(0)" ::: "memory");
; #pragma unroll
;     for (int qd = 0; qd < 8; ++qd) {
;         const int rho = 16 * qd + (lane >> 2), piece = lane & 3;
;         const u32x4 o = *(const LAS u32x4*)(scr + rho * 80 + piece * 16);
;         const int nl = 4 * (rho & 31) + (rho >> 5);
;         *(u32x4*)(WT + (size_t)(n0 + nl) * K + k0 + piece * 16) = o; }
;     asm volatile("s_waitcnt lgkmcnt(0)" ::: "memory");
; }
; __global__ void __launch_bounds__(512, 2) mega(Args a) {
;     ...
;             if (l + 1 < NLAYER && vcu >= 8) {
;                 LAS float* scr = (LAS float*)(lds + wave * 16384);
;                 for (int it = (vcu - 8) * 8 + wave; it < IT_LAYER / 2; it += (G - 8) * 8) CONVERT_ITEM(l + 1, it);
;             }
.LBB0_328:
	v_readlane_b32 s0, v255, 44
	s_nop 3
	s_cmp_eq_u32 s0, 1
	s_cbranch_scc1 .Lb_skipconv
	v_readlane_b32 s0, v248, 13
	v_readlane_b32 s2, v254, 56
	v_readlane_b32 s1, v248, 14
	v_readlane_b32 s3, v254, 57
	s_or_b64 s[0:1], s[2:3], s[0:1]
	v_readlane_b32 s2, v248, 16
	v_readlane_b32 s3, v248, 17
	s_or_b64 s[0:1], s[0:1], s[2:3]
	s_andn2_b64 vcc, exec, s[0:1]
	s_waitcnt vmcnt(0)
	s_barrier
	s_cbranch_vccz .LBB0_363
	v_ashrrev_i32_e32 v0, 1, v100
	v_lshlrev_b32_e32 v1, 4, v100
	v_and_b32_e32 v101, -16, v0
	v_ashrrev_i32_e32 v0, 2, v100
	v_and_b32_e32 v64, 48, v1
	v_and_b32_e32 v1, 0x7c, v100
	v_ashrrev_i32_e32 v6, 7, v100
	v_add_u32_e32 v102, v1, v6
	v_add_u32_e32 v6, 16, v0
	v_lshlrev_b32_e32 v7, 2, v6
	v_and_b32_e32 v7, 0x7c, v7
	v_ashrrev_i32_e32 v6, 5, v6
	v_add_u32_e32 v103, v7, v6
	v_add_u32_e32 v6, 32, v0
	v_ashrrev_i32_e32 v6, 5, v6
	v_add_u32_e32 v104, v1, v6
	v_add_u32_e32 v6, 48, v0
	v_lshlrev_b32_e32 v7, 2, v6
	v_and_b32_e32 v7, 0x7c, v7
	v_ashrrev_i32_e32 v6, 5, v6
	v_add_u32_e32 v105, v7, v6
	v_add_u32_e32 v6, 64, v0
	v_ashrrev_i32_e32 v6, 5, v6
	v_add_u32_e32 v106, v1, v6
	v_add_u32_e32 v6, 0x50, v0
	v_lshlrev_b32_e32 v7, 2, v6
	v_and_b32_e32 v7, 0x7c, v7
	v_ashrrev_i32_e32 v6, 5, v6
	s_movk_i32 s1, 0x50
	v_add_u32_e32 v107, v7, v6
	v_add_u32_e32 v6, 0x60, v0
	v_mul_lo_u32 v5, v0, s1
	v_ashrrev_i32_e32 v6, 5, v6
	v_add_u32_e32 v0, 0x70, v0
	v_add_u32_e32 v108, v1, v6
	v_lshlrev_b32_e32 v1, 2, v0
	v_and_b32_e32 v1, 0x7c, v1
	v_ashrrev_i32_e32 v0, 5, v0
	v_add_u32_e32 v109, v1, v0
	v_lshlrev_b32_e32 v0, 3, v100
	v_ashrrev_i32_e32 v110, 3, v100
	v_and_b32_e32 v152, 56, v0
	v_readlane_b32 s0, v246, 21
	v_mul_u32_u24_e32 v6, 0x84, v152
	v_lshlrev_b32_e32 v7, 2, v110
	v_add_u32_e32 v2, s0, v101
	v_add_u32_e32 v4, s0, v64
	v_add_u32_e32 v68, s0, v98
	v_add3_u32 v111, s0, v6, v7
	v_readlane_b32 s0, v255, 0
	v_mov_b32_e32 v99, v153
	v_readlane_b32 s1, v255, 1
	v_lshlrev_b32_e32 v0, 1, v152
	v_mov_b32_e32 v1, v153
	v_lshl_add_u64 v[72:73], s[0:1], 0, v[98:99]
	v_readlane_b32 s0, v255, 2
	v_readlane_b32 s1, v255, 3
	v_readlane_b32 s2, v254, 60
	v_readlane_b32 s3, v254, 61
	v_lshl_add_u64 v[74:75], s[0:1], 0, v[0:1]
	v_readlane_b32 s0, v255, 4
	v_readlane_b32 s1, v255, 5
	v_lshl_add_u64 v[66:67], s[2:3], 0, v[98:99]
	v_readlane_b32 s2, v254, 62
	v_lshl_add_u64 v[76:77], s[0:1], 0, v[98:99]
	v_readlane_b32 s0, v255, 6
	v_readlane_b32 s1, v255, 7
	v_mul_u32_u24_e32 v3, 0x50, v97
	v_readlane_b32 s3, v254, 63
	v_lshl_add_u64 v[78:79], s[0:1], 0, v[0:1]
	v_readlane_b32 s0, v255, 8
	v_readlane_b32 s1, v255, 9
	v_add_u32_e32 v84, 4, v96
	v_add_u32_e32 v86, 8, v96
	v_lshl_add_u64 v[80:81], s[0:1], 0, v[98:99]
	v_readlane_b32 s0, v255, 12
	v_readlane_b32 s1, v255, 13
	v_add_u32_e32 v88, 12, v96
	v_add_u32_e32 v90, 16, v96
	v_add_u32_e32 v92, 20, v96
	v_add_u32_e32 v94, 24, v96
	v_add_u32_e32 v100, 28, v96
	v_mov_b32_e32 v65, v153
	v_lshl_add_u64 v[70:71], s[2:3], 0, v[0:1]
	v_add_u32_e32 v112, 8, v110
	v_add_u32_e32 v113, 16, v110
	v_add_u32_e32 v114, 24, v110
	v_lshl_add_u64 v[82:83], s[0:1], 0, v[152:153]
	v_mov_b32_e32 v69, v96
	v_mov_b32_e32 v85, v84
	v_mov_b32_e32 v87, v86
	v_mov_b32_e32 v89, v88
	v_mov_b32_e32 v91, v90
	v_mov_b32_e32 v93, v92
	v_mov_b32_e32 v95, v94
	v_mov_b32_e32 v97, v100
	v_lshlrev_b32_e32 v152, 2, v98
	v_add_u32_e32 v98, v2, v3
	v_add_u32_e32 v99, v4, v5
	v_readlane_b32 s5, v248, 15
	v_readlane_b32 s0, v255, 47
	v_readlane_b32 s1, v248, 18
	s_nop 3
	s_mul_i32 s0, s0, s1
	s_add_i32 s5, s5, s0
	s_branch .LBB0_331
.LBB0_330:
	v_readlane_b32 s0, v255, 44
	s_nop 3
	s_cmp_eq_u32 s0, 5
	s_cbranch_scc1 .LBB0_363
	v_readlane_b32 s0, v248, 18
	s_add_i32 s5, s0, s5
	s_cmpk_lt_i32 s5, 0x1b78
	s_cbranch_scc0 .LBB0_363

; __global__ void __launch_bounds__(512, 2) mega(Args a) {
;     ...
;                 for (int it = (vcu - 8) * 8 + wave; it < IT_LAYER / 2; it += (G - 8) * 8) CONVERT_ITEM(l + 1, it);
;             }
;             __syncthreads();
.LBB0_363:
	v_readlane_b32 s0, v255, 44
	s_nop 3
	s_cmp_eq_u32 s0, 0
	s_cbranch_scc1 .Lb_fin
	s_cmp_eq_u32 s0, 5
	s_cbranch_scc0 .Lb_not5
	s_mov_b32 s0, 0
	v_writelane_b32 v255, s0, 44
	s_mov_b32 s0, 1
	v_writelane_b32 v255, s0, 47
	s_waitcnt vmcnt(0) lgkmcnt(0)
	s_barrier
	s_branch .LBB0_211
.Lb_not5:
	v_readlane_b32 s0, v255, 44
	s_nop 3
	s_cmp_eq_u32 s0, 2
	s_cbranch_scc0 .Lb_clr
	s_mov_b32 s0, 1
	v_writelane_b32 v255, s0, 44
	s_waitcnt vmcnt(0) lgkmcnt(0)
	s_barrier
	s_branch .Lb_reenter

; __global__ void __launch_bounds__(512, 2) mega(Args a) {
;     ...
;             __syncthreads();
.Lb_fin:
	s_mov_b32 s0, 0
	v_writelane_b32 v255, s0, 47
	s_nop 1
	s_barrier
